# P5: prefetch address math on the scalar unit (saddr loads), one shared masked-block body with diagonal-relative lane masks (no per-head mask reloads)
# speedup vs baseline: 1.0027x; 1.0027x over previous
.LBB0_541:
	v_readlane_b32 s0, v253, 12
	v_readlane_b32 s1, v253, 13
	s_mov_b64 s[4:5], s[0:1]
	s_cmp_lt_i32 s4, 6
	v_readlane_b32 s2, v253, 14
	v_readlane_b32 s3, v253, 15
	s_cselect_b64 s[0:1], -1, 0
	s_cmp_gt_i32 s5, 5
	s_cselect_b64 s[2:3], -1, 0
	s_and_b64 s[0:1], s[0:1], s[2:3]
	v_writelane_b32 v253, s0, 53
	s_andn2_b64 vcc, exec, s[0:1]
	s_nop 0
	v_writelane_b32 v253, s1, 54
	s_cbranch_vccnz .LBB0_600
	s_cmpk_gt_i32 s82, 0x3ff
	s_cbranch_scc1 .LBB0_600
	v_writelane_b32 v253, s94, 55
	s_add_u32 s0, s92, 0x66100000
	s_addc_u32 s1, s93, 0
	v_writelane_b32 v253, s95, 56
	v_writelane_b32 v253, s0, 57
	s_waitcnt vmcnt(0)
	v_lshlrev_b32_e32 v8, 4, v0
	v_lshrrev_b32_e32 v4, 2, v0
	v_writelane_b32 v253, s1, 58
	s_add_u32 s0, s92, 0x45c00000
	s_addc_u32 s1, s93, 0
	v_writelane_b32 v253, s0, 59
	v_and_b32_e32 v171, 0x78, v4
	v_or_b32_e32 v211, 7, v4
	v_writelane_b32 v253, s1, 60
	v_and_b32_e32 v215, 0x7c, v4
	v_readlane_b32 s0, v253, 18
	v_readlane_b32 s10, v253, 28
	v_readlane_b32 s1, v253, 19
	v_readlane_b32 s11, v253, 29
	s_add_u32 s0, s10, 0x6000
	s_addc_u32 s1, s11, 0
	v_readlane_b32 s2, v253, 20
	v_readlane_b32 s3, v253, 21
	v_readlane_b32 s4, v253, 22
	v_readlane_b32 s5, v253, 23
	v_readlane_b32 s6, v253, 24
	v_readlane_b32 s7, v253, 25
	v_readlane_b32 s8, v253, 26
	v_readlane_b32 s9, v253, 27
	v_readlane_b32 s12, v253, 30
	v_readlane_b32 s13, v253, 31
	v_readlane_b32 s14, v253, 32
	v_readlane_b32 s15, v253, 33
	v_writelane_b32 v253, s0, 61
	v_or_b32_e32 v220, 3, v4
	v_lshlrev_b32_e32 v4, 2, v248
	v_writelane_b32 v253, s1, 62
	s_add_u32 s0, s10, 0xc000
	s_addc_u32 s1, s11, 0
	v_writelane_b32 v253, s0, 63
	v_lshl_or_b32 v4, s84, 9, v4
	v_lshrrev_b32_e32 v12, 4, v248
	v_writelane_b32 v254, s1, 0
	s_add_u32 s0, s10, 0x12000
	s_addc_u32 s1, s11, 0
	v_writelane_b32 v254, s0, 1
	v_add_u32_e32 v221, 0, v4
	v_or_b32_e32 v4, 0x200, v0
	v_writelane_b32 v254, s1, 2
	s_add_i32 s0, 0, 0x1b800
	v_add_u32_e32 v214, s0, v8
	s_add_u32 s0, s92, 0x59c00000
	s_addc_u32 s1, s93, 0
	v_writelane_b32 v254, s0, 3
	s_cmp_gt_u32 s48, 63
	s_cselect_b64 s[4:5], -1, 0
	v_writelane_b32 v254, s1, 4
	v_cmp_gt_u32_e64 s[0:1], 2, v248
	s_cmpk_gt_u32 s48, 0x7f
	v_and_b32_e32 v1, 15, v0
	v_writelane_b32 v254, s0, 5
	v_lshrrev_b32_e32 v4, 4, v4
	v_lshlrev_b32_e32 v164, 2, v12
	v_writelane_b32 v254, s1, 6
	v_cmp_gt_u32_e64 s[0:1], 4, v248
	v_mul_u32_u24_e32 v230, 0x110, v4
	v_lshlrev_b32_e32 v4, 3, v12
	v_writelane_b32 v254, s0, 7
	v_lshl_or_b32 v232, s84, 4, v1
	v_mov_b32_e32 v198, s84
	v_lshrrev_b32_e32 v198, 1, v198
	v_lshlrev_b32_e32 v198, 5, v198
	v_sub_u32_e32 v198, v232, v198
	v_or_b32_e32 v12, 1, v164
	v_writelane_b32 v254, s1, 8
	v_cmp_gt_u32_e64 s[0:1], 8, v248
	v_cmp_eq_u32_e64 s[24:25], v12, v198
	v_or_b32_e32 v12, 3, v164
	v_writelane_b32 v254, s0, 9
	v_or_b32_e32 v13, 17, v164
	v_cmp_gt_u32_e64 s[30:31], v12, v198
	v_writelane_b32 v254, s1, 10
	v_cmp_gt_u32_e64 s[0:1], 16, v248
	v_cmp_eq_u32_e64 s[40:41], v12, v198
	v_or_b32_e32 v12, 33, v164
	v_writelane_b32 v254, s0, 11
	v_cmp_gt_u32_e64 s[18:19], v13, v198
	v_cmp_eq_u32_e64 s[26:27], v13, v198
	v_writelane_b32 v254, s1, 12
	v_cmp_gt_u32_e64 s[0:1], 32, v248
	v_or_b32_e32 v13, 2, v164
	v_or_b32_e32 v14, 16, v164
	v_writelane_b32 v254, s0, 13
	v_cmp_gt_u32_e64 s[34:35], v13, v198
	v_cmp_eq_u32_e64 s[42:43], v13, v198
	v_writelane_b32 v254, s1, 14
	v_writelane_b32 v254, s4, 15
	s_movk_i32 s0, 0x110
	v_mul_lo_u32 v9, v232, s0
	v_writelane_b32 v254, s5, 16
	s_cselect_b64 s[4:5], -1, 0
	v_writelane_b32 v254, s4, 17
	s_cmpk_gt_u32 s48, 0xbf
	v_cmp_gt_u32_e64 s[0:1], v12, v232
	v_writelane_b32 v254, s5, 18
	s_cselect_b64 s[4:5], -1, 0
	v_writelane_b32 v254, s4, 19
	s_cmpk_gt_u32 s48, 0xff
	v_or_b32_e32 v13, 32, v164
	v_writelane_b32 v254, s5, 20
	s_cselect_b64 s[4:5], -1, 0
	v_writelane_b32 v254, s4, 21
	s_cmpk_gt_u32 s48, 0x13f
	v_cmp_gt_u32_e64 s[20:21], v14, v198
	v_writelane_b32 v254, s5, 22
	s_cselect_b64 s[4:5], -1, 0
	v_writelane_b32 v254, s4, 23
	s_cmpk_gt_u32 s48, 0x17f
	v_cmp_eq_u32_e64 s[28:29], v14, v198
	v_writelane_b32 v254, s5, 24
	s_cselect_b64 s[4:5], -1, 0
	v_writelane_b32 v254, s4, 25
	s_cmpk_gt_u32 s48, 0x1bf
	v_or_b32_e32 v14, 19, v164
	v_writelane_b32 v254, s5, 26
	s_cselect_b64 s[4:5], -1, 0
	v_writelane_b32 v254, s4, 27
	v_cmp_gt_u32_e64 s[36:37], v14, v198
	v_cmp_eq_u32_e64 s[44:45], v14, v198
	v_writelane_b32 v254, s5, 28
	v_writelane_b32 v254, s0, 29
	v_or_b32_e32 v14, 49, v164
	v_or_b32_e32 v15, 18, v164
	v_writelane_b32 v254, s1, 30
	v_cmp_gt_u32_e64 s[0:1], v13, v232
	v_cmp_gt_u32_e64 s[38:39], v15, v198
	v_cmp_eq_u32_e64 s[46:47], v15, v198
	v_writelane_b32 v254, s0, 31
	v_or_b32_e32 v15, 48, v164
	v_lshlrev_b32_e32 v2, 1, v0
	v_writelane_b32 v254, s1, 32
	v_cmp_gt_u32_e64 s[0:1], v14, v232
	v_and_b32_e32 v165, 62, v2
	v_lshlrev_b32_e32 v2, 3, v0
	v_writelane_b32 v254, s0, 33
	v_and_b32_e32 v212, 0x78, v2
	v_mov_b32_e32 v161, 0
	v_writelane_b32 v254, s1, 34
	v_cmp_gt_u32_e64 s[0:1], v15, v232
	v_lshlrev_b32_e32 v158, 1, v212
	v_mov_b32_e32 v159, v161
	v_writelane_b32 v254, s0, 35
	v_lshl_add_u64 v[2:3], s[92:93], 0, v[158:159]
	s_add_i32 s33, 0, 0x13000
	v_writelane_b32 v254, s1, 36
	v_cmp_eq_u32_e64 s[0:1], v12, v232
	v_or_b32_e32 v12, 35, v164
	s_add_i32 s10, 0, 0x17400
	v_writelane_b32 v254, s0, 37
	v_and_b32_e32 v160, 0x1f00, v8
	s_cmpk_gt_u32 s48, 0x1ff
	v_writelane_b32 v254, s1, 38
	v_cmp_eq_u32_e64 s[0:1], v13, v232
	v_or_b32_e32 v13, 34, v164
	v_lshl_add_u64 v[2:3], v[2:3], 0, v[160:161]
	v_writelane_b32 v254, s0, 39
	s_cselect_b64 s[94:95], -1, 0
	v_and_b32_e32 v162, 48, v0
	v_writelane_b32 v254, s1, 40
	v_cmp_eq_u32_e64 s[0:1], v14, v232
	v_or_b32_e32 v14, 51, v164
	v_mul_u32_u24_e32 v222, 0x110, v1
	v_writelane_b32 v254, s0, 41
	v_and_b32_e32 v10, 0x1e0, v0
	v_lshrrev_b32_e32 v11, 4, v0
	v_writelane_b32 v254, s1, 42
	v_cmp_eq_u32_e64 s[0:1], v15, v232
	v_or_b32_e32 v15, 50, v164
	v_and_b32_e32 v160, 48, v248
	v_writelane_b32 v254, s0, 43
	v_readlane_b32 s48, v253, 34
	v_add_u32_e32 v159, 0, v8
	v_writelane_b32 v254, s1, 44
	v_cmp_gt_u32_e64 s[0:1], v12, v232
	v_add_u32_e32 v5, 0, v158
	v_mul_u32_u24_e32 v6, 0x110, v215
	v_writelane_b32 v254, s0, 45
	v_mul_u32_u24_e32 v7, 0x110, v220
	v_add3_u32 v223, 0, v162, v222
	v_writelane_b32 v254, s1, 46
	v_cmp_gt_u32_e64 s[0:1], v13, v232
	v_mul_u32_u24_e32 v225, 0x110, v165
	v_lshlrev_b32_e32 v226, 1, v171
	v_writelane_b32 v254, s0, 47
	v_mul_u32_u24_e32 v228, 0x110, v11
	v_add_u32_e32 v9, 0, v9
	v_writelane_b32 v254, s1, 48
	v_cmp_gt_u32_e64 s[0:1], v14, v232
	v_readlane_b32 s49, v253, 35
	v_readlane_b32 s52, v253, 38
	v_writelane_b32 v254, s0, 49
	v_readlane_b32 s53, v253, 39
	v_add_u32_e32 v242, 0, v10
	v_writelane_b32 v254, s1, 50
	v_cmp_gt_u32_e64 s[0:1], v15, v232
	s_mov_b32 s3, 0
	v_add_u32_e32 v213, 0x2000, v159
	v_writelane_b32 v254, s0, 51
	v_add_u32_e32 v208, -2, v215
	v_add_u32_e32 v209, -1, v215
	v_writelane_b32 v254, s1, 52
	v_cmp_eq_u32_e64 s[0:1], v12, v232
	v_or_b32_e32 v12, 0x41, v164
	v_cmp_eq_u32_e64 s[86:87], 0, v248
	v_writelane_b32 v254, s0, 53
	v_add_u32_e32 v224, 0xa800, v223
	v_add3_u32 v227, s33, v225, v226
	v_writelane_b32 v254, s1, 54
	v_cmp_eq_u32_e64 s[0:1], v13, v232
	v_or_b32_e32 v13, 64, v164
	v_add3_u32 v229, s10, v228, v158
	v_writelane_b32 v254, s0, 55
	v_add3_u32 v231, s10, v230, v158
	v_cmp_gt_u32_e64 s[14:15], v198, v164
	v_writelane_b32 v254, s1, 56
	v_cmp_eq_u32_e64 s[0:1], v14, v232
	v_or_b32_e32 v14, 0x51, v164
	v_cmp_gt_u32_e64 s[16:17], v164, v198
	v_writelane_b32 v254, s0, 57
	v_cmp_eq_u32_e64 s[22:23], v164, v198
	v_mov_b32_e32 v207, v248
	v_writelane_b32 v254, s1, 58
	v_cmp_eq_u32_e64 s[0:1], v15, v232
	v_or_b32_e32 v15, 0x50, v164
	v_lshl_add_u64 v[168:169], s[52:53], 0, v[160:161]
	v_writelane_b32 v254, s0, 59
	v_add_u32_e32 v243, 0x200, v242
	s_movk_i32 s11, 0x3000
	v_writelane_b32 v254, s1, 60
	v_cmp_gt_u32_e64 s[0:1], v12, v232
	s_mov_b32 s48, 0x12000
	s_mov_b32 s85, 0x41a00000
	v_writelane_b32 v254, s0, 61
	v_mov_b32_e32 v246, 0x3ecc95a3
	v_add_u32_e32 v247, v5, v6
	v_writelane_b32 v254, s1, 62
	v_cmp_gt_u32_e64 s[0:1], v13, v232
	v_add_u32_e32 v248, v5, v7
	v_add_u32_e32 v249, v9, v162
	v_writelane_b32 v254, s0, 63
	s_mov_b64 s[96:97], 0x80
	v_lshlrev_b32_e32 v172, 1, v4
	v_writelane_b32 v255, s1, 0
	v_cmp_gt_u32_e64 s[0:1], v14, v232
	v_mov_b32_e32 v250, 0x3727c5ac
	v_mov_b32_e32 v174, 0x3f317218
	v_writelane_b32 v255, s0, 1
	v_mov_b32_e32 v251, 0x7f800000
	v_mov_b32_e32 v252, 0x7fc00000
	v_writelane_b32 v255, s1, 2
	v_cmp_gt_u32_e64 s[0:1], v15, v232
	v_mov_b32_e32 v210, 0xff800000
	s_mov_b32 s49, s82
	v_writelane_b32 v255, s0, 3
	v_readlane_b32 s50, v253, 36
	v_readlane_b32 s51, v253, 37
	v_writelane_b32 v255, s1, 4
	v_cmp_eq_u32_e64 s[0:1], v12, v232
	v_or_b32_e32 v12, 0x43, v164
	v_readlane_b32 s54, v253, 40
	v_writelane_b32 v255, s0, 5
	v_readlane_b32 s55, v253, 41
	v_readlane_b32 s56, v253, 42
	v_writelane_b32 v255, s1, 6
	v_cmp_eq_u32_e64 s[0:1], v13, v232
	v_or_b32_e32 v13, 0x42, v164
	v_readlane_b32 s57, v253, 43
	v_writelane_b32 v255, s0, 7
	v_readlane_b32 s58, v253, 44
	v_readlane_b32 s59, v253, 45
	v_writelane_b32 v255, s1, 8
	v_cmp_eq_u32_e64 s[0:1], v14, v232
	v_or_b32_e32 v14, 0x53, v164
	v_readlane_b32 s60, v253, 46
	v_writelane_b32 v255, s0, 9
	v_readlane_b32 s61, v253, 47
	v_readlane_b32 s62, v253, 48
	v_writelane_b32 v255, s1, 10
	v_cmp_eq_u32_e64 s[0:1], v15, v232
	v_or_b32_e32 v15, 0x52, v164
	v_readlane_b32 s63, v253, 49
	v_writelane_b32 v255, s0, 11
	s_nop 1
	v_writelane_b32 v255, s1, 12
	v_cmp_gt_u32_e64 s[0:1], v12, v232
	s_nop 1
	v_writelane_b32 v255, s0, 13
	s_nop 1
	v_writelane_b32 v255, s1, 14
	v_cmp_gt_u32_e64 s[0:1], v13, v232
	s_nop 1
	v_writelane_b32 v255, s0, 15
	s_nop 1
	v_writelane_b32 v255, s1, 16
	v_cmp_gt_u32_e64 s[0:1], v14, v232
	s_nop 1
	v_writelane_b32 v255, s0, 17
	s_nop 1
	v_writelane_b32 v255, s1, 18
	v_cmp_gt_u32_e64 s[0:1], v15, v232
	s_nop 1
	v_writelane_b32 v255, s0, 19
	s_nop 1
	v_writelane_b32 v255, s1, 20
	v_cmp_eq_u32_e64 s[0:1], v12, v232
	v_or_b32_e32 v12, 0x61, v164
	s_nop 0
	v_writelane_b32 v255, s0, 21
	s_nop 1
	v_writelane_b32 v255, s1, 22
	v_cmp_eq_u32_e64 s[0:1], v13, v232
	v_or_b32_e32 v13, 0x60, v164
	s_nop 0
	v_writelane_b32 v255, s0, 23
	s_nop 1
	v_writelane_b32 v255, s1, 24
	v_cmp_eq_u32_e64 s[0:1], v14, v232
	v_or_b32_e32 v14, 0x71, v164
	s_nop 0
	v_writelane_b32 v255, s0, 25
	s_nop 1
	v_writelane_b32 v255, s1, 26
	v_cmp_eq_u32_e64 s[0:1], v15, v232
	v_or_b32_e32 v15, 0x70, v164
	s_nop 0
	v_writelane_b32 v255, s0, 27
	s_nop 1
	v_writelane_b32 v255, s1, 28
	v_cmp_gt_u32_e64 s[0:1], v12, v232
	s_nop 1
	v_writelane_b32 v255, s0, 29
	s_nop 1
	v_writelane_b32 v255, s1, 30
	v_cmp_gt_u32_e64 s[0:1], v13, v232
	s_nop 1
	v_writelane_b32 v255, s0, 31
	s_nop 1
	v_writelane_b32 v255, s1, 32
	v_cmp_gt_u32_e64 s[0:1], v14, v232
	s_nop 1
	v_writelane_b32 v255, s0, 33
	s_nop 1
	v_writelane_b32 v255, s1, 34
	v_cmp_gt_u32_e64 s[0:1], v15, v232
	s_nop 1
	v_writelane_b32 v255, s0, 35
	s_nop 1
	v_writelane_b32 v255, s1, 36
	v_cmp_eq_u32_e64 s[0:1], v12, v232
	v_or_b32_e32 v12, 0x63, v164
	v_cmp_eq_u32_e64 s[72:73], v12, v232
	v_writelane_b32 v255, s0, 37
	s_nop 1
	v_writelane_b32 v255, s1, 38
	v_cmp_eq_u32_e64 s[0:1], v13, v232
	v_or_b32_e32 v13, 0x62, v164
	v_cmp_eq_u32_e64 s[74:75], v13, v232
	v_writelane_b32 v255, s0, 39
	s_nop 1
	v_writelane_b32 v255, s1, 40
	v_cmp_eq_u32_e64 s[0:1], v14, v232
	v_or_b32_e32 v14, 0x73, v164
	v_cmp_eq_u32_e64 s[76:77], v14, v232
	v_writelane_b32 v255, s0, 41
	s_nop 1
	v_writelane_b32 v255, s1, 42
	v_cmp_eq_u32_e64 s[0:1], v15, v232
	v_or_b32_e32 v15, 0x72, v164
	v_cmp_eq_u32_e64 s[78:79], v15, v232
	v_writelane_b32 v255, s0, 43
	s_nop 1
	v_writelane_b32 v255, s1, 44
	v_cmp_gt_u32_e64 s[0:1], v12, v232
	v_mbcnt_lo_u32_b32 v12, -1, 0
	v_mbcnt_hi_u32_b32 v12, -1, v12
	v_writelane_b32 v255, s0, 45
	s_nop 1
	v_writelane_b32 v255, s1, 46
	v_cmp_gt_u32_e64 s[0:1], v13, v232
	v_and_b32_e32 v13, 64, v12
	s_nop 0
	v_writelane_b32 v255, s0, 47
	s_nop 1
	v_writelane_b32 v255, s1, 48
	v_cmp_gt_u32_e64 s[0:1], v14, v232
	v_bfrev_b32_e32 v14, 0.5
	v_lshl_or_b32 v233, v12, 2, v14
	v_add_u32_e32 v14, -1, v12
	v_cmp_lt_i32_e32 vcc, v14, v13
	v_writelane_b32 v255, s0, 49
	s_nop 0
	v_cndmask_b32_e32 v14, v14, v12, vcc
	v_lshlrev_b32_e32 v234, 2, v14
	v_add_u32_e32 v14, -2, v12
	v_cmp_lt_i32_e32 vcc, v14, v13
	v_writelane_b32 v255, s1, 50
	v_cmp_gt_u32_e64 s[0:1], v15, v232
	v_cndmask_b32_e32 v14, v14, v12, vcc
	v_lshlrev_b32_e32 v235, 2, v14
	v_add_u32_e32 v14, -4, v12
	v_cmp_lt_i32_e32 vcc, v14, v13
	v_writelane_b32 v255, s0, 51
	s_nop 0
	v_cndmask_b32_e32 v14, v14, v12, vcc
	v_lshlrev_b32_e32 v236, 2, v14
	v_add_u32_e32 v14, -8, v12
	v_cmp_lt_i32_e32 vcc, v14, v13
	v_writelane_b32 v255, s1, 52
	s_mov_b64 s[0:1], 0x5e000000
	v_cndmask_b32_e32 v14, v14, v12, vcc
	v_lshlrev_b32_e32 v237, 2, v14
	v_add_u32_e32 v14, -16, v12
	v_cmp_lt_i32_e32 vcc, v14, v13
	v_lshl_add_u64 v[166:167], v[2:3], 0, s[0:1]
	s_lshl_b32 s0, s84, 6
	v_cndmask_b32_e32 v14, v14, v12, vcc
	v_lshlrev_b32_e32 v238, 2, v14
	v_subrev_u32_e32 v14, 32, v12
	v_cmp_lt_i32_e32 vcc, v14, v13
	s_add_i32 s0, s0, 0
	v_add_u32_e32 v13, 64, v13
	v_cndmask_b32_e32 v14, v14, v12, vcc
	v_lshlrev_b32_e32 v239, 2, v14
	v_xor_b32_e32 v14, 16, v12
	v_lshl_add_u32 v245, v1, 2, s0
	s_add_u32 s0, s12, 0x100
	v_cmp_lt_i32_e32 vcc, v14, v13
	s_addc_u32 s1, s13, 0
	v_writelane_b32 v255, s0, 53
	v_cndmask_b32_e32 v14, v12, v14, vcc
	v_lshlrev_b32_e32 v240, 2, v14
	v_xor_b32_e32 v14, 32, v12
	v_writelane_b32 v255, s1, 54
	v_cmp_lt_i32_e32 vcc, v14, v13
	v_lshlrev_b32_e32 v2, 4, v1
	v_writelane_b32 v255, s82, 55
	v_cndmask_b32_e32 v12, v12, v14, vcc
	v_lshl_or_b32 v170, v11, 8, v2
	v_add_u32_e32 v2, 0, v160
	v_writelane_b32 v255, s82, 56
	v_lshlrev_b32_e32 v241, 2, v12
	v_add_u32_e32 v244, 0x1000, v2
	s_movk_i32 s12, 0x6000
	s_mov_b32 s13, 0xc000
	v_writelane_b32 v255, s83, 57
	s_branch .LBB0_545

.LBB0_565:
	v_lshl_add_u64 v[128:129], s[92:93], 0, v[126:127]
	s_mov_b32 s4, 0x3dc00000
	v_add_co_u32_e32 v198, vcc, s4, v128
	v_readlane_b32 s6, v11, s2
	s_nop 0
	v_addc_co_u32_e32 v199, vcc, 0, v129, vcc
	v_mov_b64_e32 v[74:75], v[200:201]
	v_mov_b64_e32 v[76:77], v[202:203]
	v_mov_b64_e32 v[70:71], v[216:217]
	v_mov_b64_e32 v[72:73], v[218:219]
	global_load_dwordx4 v[200:203], v[198:199], off offset:128
	global_load_dwordx4 v[216:219], v[198:199], off offset:192
	s_cmpk_eq_i32 s0, 0x700
	s_cbranch_scc1 .Lp5_pf_skip
	global_load_dword v2, v124, s[92:93]
	global_load_dword v1, v122, s[92:93]
	global_load_dword v12, v120, s[92:93]
	s_add_u32 s4, s92, 0x45c00000
	s_addc_u32 s5, s93, 0
	global_load_dword v3, v118, s[4:5] offset:128
	s_add_u32 s4, s4, 0x3000
	s_addc_u32 s5, s5, 0
	global_load_dword v4, v118, s[4:5] offset:128
	s_add_u32 s4, s4, 0x3000
	s_addc_u32 s5, s5, 0
	global_load_dword v5, v118, s[4:5] offset:128
	s_add_u32 s4, s4, 0x3000
	s_addc_u32 s5, s5, 0
	global_load_dword v6, v118, s[4:5] offset:128
	s_add_u32 s4, s4, 0x3000
	s_addc_u32 s5, s5, 0
	global_load_dword v7, v118, s[4:5] offset:128
	s_add_u32 s4, s4, 0x3000
	s_addc_u32 s5, s5, 0
	global_load_dword v8, v118, s[4:5] offset:128
	s_add_u32 s4, s4, 0x3000
	s_addc_u32 s5, s5, 0
	global_load_dword v9, v118, s[4:5] offset:128
	global_load_dword v10, v116, s[92:93]
	v_lshl_add_u64 v[14:15], v[110:111], 0, s[0:1]
	s_movk_i32 s4, 0x6000
	s_mov_b32 s5, 0
	global_load_dwordx2 v[176:177], v[14:15], off offset:256
	v_lshl_add_u64 v[14:15], v[14:15], 0, s[4:5]
	global_load_dwordx2 v[178:179], v[14:15], off offset:256
	v_lshl_add_u64 v[14:15], v[14:15], 0, s[4:5]
	global_load_dwordx2 v[180:181], v[14:15], off offset:256
	v_lshl_add_u64 v[14:15], v[14:15], 0, s[4:5]
	global_load_dwordx2 v[182:183], v[14:15], off offset:256
	v_lshl_add_u64 v[14:15], v[112:113], 0, s[0:1]
	global_load_dwordx2 v[184:185], v[14:15], off
	v_lshl_add_u64 v[94:95], s[92:93], 0, v[114:115]
	s_mov_b32 s4, 0x5e004000
	v_lshl_add_u64 v[16:17], v[94:95], 0, s[4:5]
	global_load_dwordx4 v[14:17], v[16:17], off
	s_mov_b32 s4, 0x5e006000
	v_lshl_add_u64 v[18:19], v[94:95], 0, s[4:5]
	global_load_dwordx4 v[18:21], v[18:19], off

.LBB0_583:
	s_andn2_b64 vcc, exec, s[4:5]
	s_cbranch_vccnz .LBB0_585
	v_max_f32_e32 v132, v151, v151
	v_min_f32_e32 v132, 0, v132
	v_min_f32_e32 v133, 0, v149
	v_mul_f32_e32 v132, 0x3fb8aa3b, v132
	v_mul_f32_e32 v133, 0x3fb8aa3b, v133
	v_min_f32_e32 v134, 0, v150
	v_min_f32_e32 v135, 0, v148
	v_exp_f32_e32 v132, v132
	v_exp_f32_e32 v133, v133
	v_mul_f32_e32 v134, 0x3fb8aa3b, v134
	v_mul_f32_e32 v135, 0x3fb8aa3b, v135
	v_exp_f32_e32 v134, v134
	v_exp_f32_e32 v135, v135
	v_mul_f32_e32 v132, v50, v132
	v_mul_f32_e32 v133, v51, v133
	v_cndmask_b32_e64 v132, v132, 0, s[16:17]
	v_cndmask_b32_e64 v133, 0, v133, s[14:15]
	v_pk_mul_f32 v[134:135], v[42:43], v[134:135]
	v_pk_add_f32 v[136:137], v[130:131], v[132:133] op_sel_hi:[0,1]
	v_cndmask_b32_e64 v135, v135, 0, s[18:19]
	v_cndmask_b32_e64 v134, v134, 0, s[20:21]
	v_cndmask_b32_e64 v133, v133, v137, s[24:25]
	v_cndmask_b32_e64 v132, v132, v136, s[22:23]
	v_pk_add_f32 v[136:137], v[130:131], v[134:135] op_sel_hi:[0,1]
	v_cndmask_b32_e64 v135, v135, v137, s[26:27]
	v_min_f32_e32 v137, 0, v146
	v_mul_f32_e32 v137, 0x3fb8aa3b, v137
	v_cndmask_b32_e64 v134, v134, v136, s[28:29]
	v_min_f32_e32 v136, 0, v147
	v_exp_f32_e32 v138, v137
	v_min_f32_e32 v137, 0, v145
	v_mul_f32_e32 v136, 0x3fb8aa3b, v136
	v_mul_f32_e32 v137, 0x3fb8aa3b, v137
	v_min_f32_e32 v139, 0, v144
	v_exp_f32_e32 v136, v136
	v_exp_f32_e32 v137, v137
	v_mul_f32_e32 v139, 0x3fb8aa3b, v139
	v_exp_f32_e32 v139, v139
	v_pk_mul_f32 v[136:137], v[52:53], v[136:137]
	s_nop 0
	v_cndmask_b32_e64 v137, v137, 0, s[30:31]
	v_cndmask_b32_e64 v136, v136, 0, s[34:35]
	v_pk_mul_f32 v[138:139], v[44:45], v[138:139]
	v_pk_add_f32 v[144:145], v[130:131], v[136:137] op_sel_hi:[0,1]
	v_cndmask_b32_e64 v139, v139, 0, s[36:37]
	v_cndmask_b32_e64 v138, v138, 0, s[38:39]
	v_cndmask_b32_e64 v137, v137, v145, s[40:41]
	v_cndmask_b32_e64 v136, v136, v144, s[42:43]
	v_pk_add_f32 v[144:145], v[130:131], v[138:139] op_sel_hi:[0,1]
	v_cndmask_b32_e64 v139, v139, v145, s[44:45]
	v_cndmask_b32_e64 v138, v138, v144, s[46:47]

.LBB0_588:
	s_andn2_b64 vcc, exec, s[4:5]
	s_cbranch_vccnz .LBB0_590
	v_max_f32_e32 v132, v151, v151
	v_min_f32_e32 v132, 0, v132
	v_min_f32_e32 v133, 0, v149
	v_mul_f32_e32 v132, 0x3fb8aa3b, v132
	v_mul_f32_e32 v133, 0x3fb8aa3b, v133
	v_min_f32_e32 v134, 0, v150
	v_min_f32_e32 v135, 0, v148
	v_exp_f32_e32 v132, v132
	v_exp_f32_e32 v133, v133
	v_mul_f32_e32 v134, 0x3fb8aa3b, v134
	v_mul_f32_e32 v135, 0x3fb8aa3b, v135
	v_exp_f32_e32 v134, v134
	v_exp_f32_e32 v135, v135
	v_mul_f32_e32 v132, v58, v132
	v_mul_f32_e32 v133, v59, v133
	v_cndmask_b32_e64 v132, v132, 0, s[16:17]
	v_cndmask_b32_e64 v133, 0, v133, s[14:15]
	v_pk_mul_f32 v[134:135], v[54:55], v[134:135]
	v_pk_add_f32 v[136:137], v[130:131], v[132:133] op_sel_hi:[0,1]
	v_cndmask_b32_e64 v135, v135, 0, s[18:19]
	v_cndmask_b32_e64 v134, v134, 0, s[20:21]
	v_cndmask_b32_e64 v133, v133, v137, s[24:25]
	v_cndmask_b32_e64 v132, v132, v136, s[22:23]
	v_pk_add_f32 v[136:137], v[130:131], v[134:135] op_sel_hi:[0,1]
	v_cndmask_b32_e64 v135, v135, v137, s[26:27]
	v_min_f32_e32 v137, 0, v146
	v_mul_f32_e32 v137, 0x3fb8aa3b, v137
	v_cndmask_b32_e64 v134, v134, v136, s[28:29]
	v_min_f32_e32 v136, 0, v147
	v_exp_f32_e32 v138, v137
	v_min_f32_e32 v137, 0, v145
	v_mul_f32_e32 v136, 0x3fb8aa3b, v136
	v_mul_f32_e32 v137, 0x3fb8aa3b, v137
	v_min_f32_e32 v139, 0, v144
	v_exp_f32_e32 v136, v136
	v_exp_f32_e32 v137, v137
	v_mul_f32_e32 v139, 0x3fb8aa3b, v139
	v_exp_f32_e32 v139, v139
	v_pk_mul_f32 v[136:137], v[60:61], v[136:137]
	s_nop 0
	v_cndmask_b32_e64 v137, v137, 0, s[30:31]
	v_cndmask_b32_e64 v136, v136, 0, s[34:35]
	v_pk_mul_f32 v[138:139], v[56:57], v[138:139]
	v_pk_add_f32 v[144:145], v[130:131], v[136:137] op_sel_hi:[0,1]
	v_cndmask_b32_e64 v139, v139, 0, s[36:37]
	v_cndmask_b32_e64 v138, v138, 0, s[38:39]
	v_cndmask_b32_e64 v137, v137, v145, s[40:41]
	v_cndmask_b32_e64 v136, v136, v144, s[42:43]
	v_pk_add_f32 v[144:145], v[130:131], v[138:139] op_sel_hi:[0,1]
	v_cndmask_b32_e64 v139, v139, v145, s[44:45]
	v_cndmask_b32_e64 v138, v138, v144, s[46:47]

.LBB0_593:
	s_andn2_b64 vcc, exec, s[4:5]
	s_cbranch_vccnz .LBB0_595
	v_max_f32_e32 v132, v149, v149
	v_min_f32_e32 v132, 0, v132
	v_min_f32_e32 v133, 0, v148
	v_mul_f32_e32 v132, 0x3fb8aa3b, v132
	v_mul_f32_e32 v133, 0x3fb8aa3b, v133
	v_min_f32_e32 v134, 0, v150
	v_min_f32_e32 v135, 0, v147
	v_exp_f32_e32 v132, v132
	v_exp_f32_e32 v133, v133
	v_mul_f32_e32 v134, 0x3fb8aa3b, v134
	v_mul_f32_e32 v135, 0x3fb8aa3b, v135
	v_exp_f32_e32 v134, v134
	v_exp_f32_e32 v135, v135
	v_mul_f32_e32 v132, v66, v132
	v_mul_f32_e32 v133, v67, v133
	v_cndmask_b32_e64 v132, v132, 0, s[16:17]
	v_cndmask_b32_e64 v133, 0, v133, s[14:15]
	v_pk_mul_f32 v[134:135], v[62:63], v[134:135]
	v_pk_add_f32 v[136:137], v[130:131], v[132:133] op_sel_hi:[0,1]
	v_cndmask_b32_e64 v135, v135, 0, s[18:19]
	v_cndmask_b32_e64 v134, v134, 0, s[20:21]
	v_cndmask_b32_e64 v133, v133, v137, s[24:25]
	v_cndmask_b32_e64 v132, v132, v136, s[22:23]
	v_pk_add_f32 v[136:137], v[130:131], v[134:135] op_sel_hi:[0,1]
	v_cndmask_b32_e64 v135, v135, v137, s[26:27]
	v_min_f32_e32 v137, 0, v145
	v_mul_f32_e32 v137, 0x3fb8aa3b, v137
	v_cndmask_b32_e64 v134, v134, v136, s[28:29]
	v_min_f32_e32 v136, 0, v146
	v_exp_f32_e32 v138, v137
	v_min_f32_e32 v137, 0, v144
	v_mul_f32_e32 v136, 0x3fb8aa3b, v136
	v_mul_f32_e32 v137, 0x3fb8aa3b, v137
	v_min_f32_e32 v139, 0, v143
	v_exp_f32_e32 v136, v136
	v_exp_f32_e32 v137, v137
	v_mul_f32_e32 v139, 0x3fb8aa3b, v139
	v_exp_f32_e32 v139, v139
	v_pk_mul_f32 v[136:137], v[68:69], v[136:137]
	s_nop 0
	v_cndmask_b32_e64 v137, v137, 0, s[30:31]
	v_cndmask_b32_e64 v136, v136, 0, s[34:35]
	v_pk_mul_f32 v[138:139], v[64:65], v[138:139]
	v_pk_add_f32 v[144:145], v[130:131], v[136:137] op_sel_hi:[0,1]
	v_cndmask_b32_e64 v139, v139, 0, s[36:37]
	v_cndmask_b32_e64 v138, v138, 0, s[38:39]
	v_cndmask_b32_e64 v137, v137, v145, s[40:41]
	v_cndmask_b32_e64 v136, v136, v144, s[42:43]
	v_pk_add_f32 v[144:145], v[130:131], v[138:139] op_sel_hi:[0,1]
	v_cndmask_b32_e64 v139, v139, v145, s[44:45]
	v_cndmask_b32_e64 v138, v138, v144, s[46:47]
